# dedicated conversion workgroups: blockIdx mod 9 (29)
# baseline (speedup 1.0000x reference)
.LBB0_454:
	s_cmp_gt_i32 s56, 3
	s_cselect_b64 s[0:1], -1, 0
	s_cmp_lt_i32 s57, 4
	s_cselect_b64 s[2:3], -1, 0
	s_or_b64 s[0:1], s[0:1], s[2:3]
	s_and_b64 vcc, exec, s[0:1]
	s_mul_i32 s46, s87, 0x38e38e39
	s_cbranch_vccnz .LBB0_616
	s_mov_b32 s1, s46
	s_mov_b32 s0, 0x1c71c71c
	v_mov_b32_e32 v2, s1
	v_mov_b32_e32 v1, v0
	v_cmp_lt_u32_e32 vcc, s0, v2
	s_nop 0
	v_cmp_eq_u32_e64 s[0:1], 0, v1
	s_cbranch_vccnz .LBB0_472
	s_mul_i32 s2, s91, 0x4100
	s_add_i32 s2, s2, 0
	s_add_u32 s10, s92, 0xa000000
	s_waitcnt lgkmcnt(0)
	v_and_b32_e32 v3, 7, v1
	v_bfe_u32 v7, v1, 3, 3
	s_addc_u32 s11, s93, 0
	v_lshlrev_b32_e32 v2, 2, v7
	v_mul_u32_u24_e32 v4, 0x810, v3
	v_add3_u32 v8, s2, v2, v4
	v_lshl_add_u32 v4, v3, 6, s2
	s_waitcnt vmcnt(0)
	v_mul_u32_u24_e32 v13, 0x204, v7
	s_add_u32 s12, s92, 0x2000000
	v_mov_b32_e32 v5, 0
	s_addc_u32 s13, s93, 0
	s_add_i32 s15, 0, 0x27c00
	v_add_u32_e32 v13, v4, v13
	s_mov_b32 s3, 0
	v_lshlrev_b32_e32 v6, 2, v3
	v_lshlrev_b32_e32 v2, 4, v3
	v_mov_b32_e32 v3, v5
	v_or_b32_e32 v9, 8, v7
	v_or_b32_e32 v10, 16, v7
	v_or_b32_e32 v11, 24, v7
	s_movk_i32 s14, 0x3ff
	v_mov_b32_e32 v12, s15
	s_movk_i32 s16, 0xbff
	s_mov_b32 s17, 0x8000
	s_mov_b32 s18, 0x10000
	s_mov_b32 s19, 0x18000
	s_mov_b32 s20, 0x20000
	s_mov_b32 s21, 0x28000
	s_mov_b32 s22, 0x30000
	s_mov_b32 s23, 0x38000
	s_mov_b32 s24, 0x40000
	s_mov_b32 s25, 0x48000
	s_mov_b32 s26, 0x50000
	s_mov_b32 s27, 0x58000
	s_mov_b32 s28, 0x60000
	s_mov_b32 s29, 0x68000
	s_mov_b32 s30, 0x70000
	s_mov_b32 s31, 0x78000
	s_mov_b32 s33, 0xc3e00000
	v_add_u32_e32 v14, 0x1020, v13
	v_add_u32_e32 v15, 0x1028, v13
	v_add_u32_e32 v16, 0x1030, v13
	v_add_u32_e32 v17, 0x1038, v13
	v_add_u32_e32 v18, 0x1040, v13
	v_add_u32_e32 v19, 0x1048, v13
	v_add_u32_e32 v20, 0x1050, v13
	v_add_u32_e32 v21, 0x1058, v13
	v_add_u32_e32 v22, 0x2040, v13
	v_add_u32_e32 v23, 0x2048, v13
	v_add_u32_e32 v24, 0x2050, v13
	v_add_u32_e32 v25, 0x2058, v13
	v_add_u32_e32 v26, 0x2060, v13
	v_add_u32_e32 v27, 0x2068, v13
	v_add_u32_e32 v28, 0x2070, v13
	v_add_u32_e32 v29, 0x2078, v13
	v_add_u32_e32 v30, 0x3060, v13
	v_add_u32_e32 v31, 0x3068, v13
	v_add_u32_e32 v32, 0x3070, v13
	v_add_u32_e32 v33, 0x3078, v13
	v_add_u32_e32 v34, 0x3080, v13
	v_add_u32_e32 v35, 0x3088, v13
	v_add_u32_e32 v36, 0x3090, v13
	v_add_u32_e32 v37, 0x3098, v13
	s_mov_b32 s34, 0x80000
	s_mov_b32 s35, 0x90000
	s_mov_b32 s38, 0xa0000
	s_mov_b32 s39, 0xb0000
	s_mov_b32 s40, 0xc0000
	s_mov_b32 s41, 0xd0000
	s_mov_b32 s42, 0xe0000
	s_mov_b32 s43, 0xf0000
	v_add_u32_e32 v38, 0x400, v8
	v_mov_b32_e32 v39, 0x43e00000
	s_branch .LBB0_459

.LBB0_616:
	s_cmp_gt_i32 s56, 4
	s_cselect_b64 s[0:1], -1, 0
	s_cmp_lt_i32 s57, 5
	s_cselect_b64 s[2:3], -1, 0
	s_or_b64 s[0:1], s[0:1], s[2:3]
	s_and_b64 vcc, exec, s[0:1]
	s_cbranch_vccnz .LBB0_749
	s_nop 0
	v_mov_b32_e32 v6, v0
	s_mov_b32 s0, 0x1c71c71c
	v_mov_b32_e32 v2, s46
	v_cmp_lt_u32_e32 vcc, s0, v2
	v_and_b32_e32 v1, 63, v6
	s_and_b64 vcc, exec, vcc
	v_cmp_eq_u32_e64 s[0:1], 0, v6
	s_mul_i32 s14, s91, 0x4100
	v_and_b32_e32 v171, 7, v6
	v_lshrrev_b32_e32 v1, 3, v1
	s_cbranch_vccnz .LBB0_634
	s_add_i32 s2, s14, 0
	s_add_u32 s10, s92, 0xa000000
	s_addc_u32 s11, s93, 0
	v_lshlrev_b32_e32 v2, 2, v1
	s_waitcnt lgkmcnt(0)
	v_mul_u32_u24_e32 v3, 0x810, v171
	v_lshl_add_u32 v4, v171, 6, s2
	s_waitcnt vmcnt(0)
	v_mul_u32_u24_e32 v13, 0x204, v1
	s_add_u32 s12, s92, 0x2000000
	v_add3_u32 v8, s2, v2, v3
	v_mov_b32_e32 v5, 0
	s_addc_u32 s13, s93, 0
	s_add_i32 s16, 0, 0x27c00
	v_add_u32_e32 v13, v4, v13
	s_mov_b32 s3, 0
	v_lshlrev_b32_e32 v7, 2, v171
	v_lshlrev_b32_e32 v2, 4, v171
	v_mov_b32_e32 v3, v5
	v_or_b32_e32 v9, 8, v1
	v_or_b32_e32 v10, 16, v1
	v_or_b32_e32 v11, 24, v1
	s_movk_i32 s15, 0x1ff
	v_mov_b32_e32 v12, s16
	s_movk_i32 s17, 0xbff
	s_mov_b32 s18, 0x8000
	s_mov_b32 s19, 0x10000
	s_mov_b32 s20, 0x18000
	s_mov_b32 s21, 0x20000
	s_mov_b32 s22, 0x28000
	s_mov_b32 s23, 0x30000
	s_mov_b32 s24, 0x38000
	s_mov_b32 s25, 0x40000
	s_mov_b32 s26, 0x48000
	s_mov_b32 s27, 0x50000
	s_mov_b32 s28, 0x58000
	s_mov_b32 s29, 0x60000
	s_mov_b32 s30, 0x68000
	s_mov_b32 s31, 0x70000
	s_mov_b32 s33, 0x78000
	s_mov_b32 s34, 0xc3e00000
	v_add_u32_e32 v14, 0x1020, v13
	v_add_u32_e32 v15, 0x1028, v13
	v_add_u32_e32 v16, 0x1030, v13
	v_add_u32_e32 v17, 0x1038, v13
	v_add_u32_e32 v18, 0x1040, v13
	v_add_u32_e32 v19, 0x1048, v13
	v_add_u32_e32 v20, 0x1050, v13
	v_add_u32_e32 v21, 0x1058, v13
	v_add_u32_e32 v22, 0x2040, v13
	v_add_u32_e32 v23, 0x2048, v13
	v_add_u32_e32 v24, 0x2050, v13
	v_add_u32_e32 v25, 0x2058, v13
	v_add_u32_e32 v26, 0x2060, v13
	v_add_u32_e32 v27, 0x2068, v13
	v_add_u32_e32 v28, 0x2070, v13
	v_add_u32_e32 v29, 0x2078, v13
	v_add_u32_e32 v30, 0x3060, v13
	v_add_u32_e32 v31, 0x3068, v13
	v_add_u32_e32 v32, 0x3070, v13
	v_add_u32_e32 v33, 0x3078, v13
	v_add_u32_e32 v34, 0x3080, v13
	v_add_u32_e32 v35, 0x3088, v13
	v_add_u32_e32 v36, 0x3090, v13
	v_add_u32_e32 v37, 0x3098, v13
	s_mov_b32 s35, 0x80000
	s_mov_b32 s38, 0x90000
	s_mov_b32 s39, 0xa0000
	s_mov_b32 s40, 0xb0000
	s_mov_b32 s41, 0xc0000
	s_mov_b32 s42, 0xd0000
	s_mov_b32 s43, 0xe0000
	s_mov_b32 s44, 0xf0000
	v_add_u32_e32 v38, 0x400, v8
	v_mov_b32_e32 v39, 0x43e00000
	s_branch .LBB0_621
